# both attention bodies: K/V tiles staged by LDS-DMA (global_load_lds), no VGPR staging / ds_write
# speedup vs baseline: 1.0215x; 1.0151x over previous
; __device__ __forceinline__ int v_st(int k, int c) { const int kk = (k & ~0xC) | ((k & 4) << 1) | ((k & 8) >> 1); return ((kk >> 3) * 4 + (c >> 5)) * 512 + ((kk & 7) * 32 + (c & 31)) * 2; }
; __device__ __forceinline__ int v_rd_base(int lane) { return ((lane & 3) << 3) | (((lane >> 2) & 3) << 6) | (((lane >> 4) & 1) << 5) | (((lane >> 5) & 1) << 8); }
; #define SWRITE(b, i) do { *(LAS bf16x8*)(V_lds + (b) * SHM_V + vst0) = sr_[i].vs0;          \
;     *(LAS bf16x8*)(V_lds + (b) * SHM_V + vst1) = sr_[i].vs1; int kc = sc * 2;               \
;     *(LAS bf16x8*)(K_lds + (b) * SHM_K + KSWZ(sr, kc)) = sr_[i].ks0;                       \
;     *(LAS bf16x8*)(K_lds + (b) * SHM_K + KSWZ(32 + sr, kc)) = sr_[i].ks1; } while (0)
; #define SWAIT() asm volatile("s_waitcnt vmcnt(4)" ::: "memory")
; template <bool HALF> __device__ __forceinline__ void dense_body(const bf16_t* __restrict__ Qb, const bf16_t* __restrict__ Kh, const bf16_t* __restrict__ Vh, ...
;     ...
;   const int sr = tid >> 4, sc = (tid & 15) * 8, vst0 = v_st(sr, sc), vst1 = v_st(32 + sr, sc);
;   const int vb0 = (int)(uintptr_t)V_lds + v_rd_base(lane);
;   struct { bf16x8 vs0, vs1, ks0, ks1; } sr_[2];
;   const unsigned ko0 = (unsigned)(sr * LDKK + sc) * 2u, ko1 = ko0 + 32u * LDKK * 2u, vo0 = (unsigned)(sr * LDKV + sc) * 2u, vo1 = vo0 + 32u * LDKV * 2u;
;     ...
;   f32x16 pA0, pA1, pB0, pB1; float mnA, mnB, alA, alB; bf16x8 pa0, pa1, pa2, pa3; const int NT = seq / KVBLK;
;   const char* Kl0 = (const char*)K_lds; const char* Kl1 = (const char*)(K_lds + SHM_K);
;   constexpr int SE = 0, SO = 1;
;   SLOAD(SE, 0); asm volatile("s_waitcnt vmcnt(0)" ::: "memory"); SWRITE(0, SE); __syncthreads();
;   qkt<HALF>(pA0, pA1, Kl0, qr, r32, hi, koff); partialSM(pA0, pA1, m_reg, mnA, alA);
;   SLOAD(SO, KVBLK); if (2 < NT) SLOAD(SE, 2 * KVBLK);
;   SWAIT(); SWRITE(1, SO); __syncthreads();
.LBB0_424:
	s_ashr_i32 s6, s2, 2
	s_add_i32 s2, s2, -8
	s_lshr_b32 s2, s2, 1
	s_add_i32 s7, s2, 2
	s_and_b64 s[2:3], s[20:21], exec
	s_cselect_b32 s3, s6, s7
	s_lshl_b32 s2, s3, 7
	s_cmp_lt_i32 s3, 2
	s_movk_i32 s3, 0x1100
	s_cselect_b32 s3, s3, 0x1500
	s_add_i32 s6, s3, s2
	s_ashr_i32 s3, s2, 31
	s_lshl_b64 s[20:21], s[2:3], 1
	s_add_u32 s34, s44, s20
	v_cvt_pk_bf16_f32 v118, v122, v36
	v_cvt_pk_bf16_f32 v119, v123, v37
	v_cvt_pk_bf16_f32 v120, v120, v28
	v_cvt_pk_bf16_f32 v121, v121, v29
	v_cvt_pk_bf16_f32 v126, v114, v32
	v_cvt_pk_bf16_f32 v127, v115, v33
	v_cvt_pk_bf16_f32 v128, v112, v24
	v_cvt_pk_bf16_f32 v129, v113, v25
	v_cvt_pk_bf16_f32 v122, v108, v26
	v_cvt_pk_bf16_f32 v123, v109, v27
	v_cvt_pk_bf16_f32 v124, v106, v20
	v_cvt_pk_bf16_f32 v125, v107, v21
	v_cvt_pk_bf16_f32 v114, v104, v22
	v_cvt_pk_bf16_f32 v115, v105, v23
	v_cvt_pk_bf16_f32 v116, v74, v16
	v_cvt_pk_bf16_f32 v117, v75, v17
	v_ashrrev_i32_e32 v16, 4, v142
	v_lshlrev_b32_e32 v17, 3, v142
	s_movk_i32 s2, 0x300
	s_addc_u32 s35, s45, s21
	s_ashr_i32 s7, s6, 31
	v_cvt_pk_bf16_f32 v110, v72, v18
	v_and_b32_e32 v18, 0x78, v17
	v_mul_lo_u32 v0, v16, s2
	s_movk_i32 s2, 0x1800
	s_lshl_b64 s[22:23], s[6:7], 1
	v_cvt_pk_bf16_f32 v111, v73, v19
	v_cvt_pk_bf16_f32 v112, v70, v12
	v_cvt_pk_bf16_f32 v113, v71, v13
	v_cvt_pk_bf16_f32 v106, v68, v14
	v_cvt_pk_bf16_f32 v107, v69, v15
	v_cvt_pk_bf16_f32 v108, v6, v8
	v_or_b32_e32 v8, v0, v18
	v_mul_lo_u32 v0, v16, s2
	s_add_u32 s38, s30, s22
	v_or_b32_e32 v0, v0, v18
	s_addc_u32 s39, s31, s23
	v_lshlrev_b32_e32 v50, 1, v0
	v_cvt_pk_bf16_f32 v109, v7, v9
	v_cvt_pk_bf16_f32 v102, v4, v10
	v_cvt_pk_bf16_f32 v103, v5, v11
	v_cvt_pk_bf16_f32 v104, v2, v64
	v_cvt_pk_bf16_f32 v105, v1, v65
	v_cvt_pk_bf16_f32 v98, v40, v46
	v_cvt_pk_bf16_f32 v99, v39, v47
	v_cvt_pk_bf16_f32 v100, v34, v42
	v_cvt_pk_bf16_f32 v101, v31, v43
	v_add_u32_e32 v48, 0x60000, v50
	v_readlane_b32 s52, v252, 4
	s_nop 3
	v_and_b32_e32 v134, 63, v142
	v_lshrrev_b32_e32 v135, 4, v134
	v_and_b32_e32 v136, 15, v134
	s_lshl_b32 s53, s52, 3
	v_add_u32_e32 v137, s53, v135
	v_xor_b32_e32 v138, v136, v135
	v_mul_u32_u24_e32 v130, 0x600, v137
	v_lshl_add_u32 v130, v138, 4, v130
	v_add_u32_e32 v139, 4, v135
	v_xor_b32_e32 v138, v136, v139
	v_add_u32_e32 v137, 4, v137
	v_mul_u32_u24_e32 v131, 0x600, v137
	v_lshl_add_u32 v131, v138, 4, v131
	v_bfe_u32 v135, v134, 2, 3
	v_add_u32_e32 v135, s53, v135
	v_and_b32_e32 v136, 4, v135
	v_and_b32_e32 v137, 8, v135
	v_and_b32_e32 v135, 0xfffffff3, v135
	v_lshl_or_b32 v135, v136, 1, v135
	v_lshrrev_b32_e32 v137, 1, v137
	v_or_b32_e32 v135, v135, v137
	v_mul_u32_u24_e32 v132, 0x3000, v135
	v_lshrrev_b32_e32 v136, 5, v134
	v_lshl_add_u32 v132, v136, 6, v132
	v_and_b32_e32 v136, 3, v134
	v_lshl_add_u32 v132, v136, 4, v132
	v_add_u32_e32 v133, 0x80, v132
	s_lshl_b32 s53, s52, 11
	s_add_i32 s52, s53, 0x8000
	s_add_i32 m0, s52, 0x0
	s_nop 0
	global_load_lds_dwordx4 v130, s[34:35]
	s_add_i32 m0, s52, 0x400
	s_nop 0
	global_load_lds_dwordx4 v131, s[34:35]
	s_add_i32 m0, s53, 0x0
	s_nop 0
	global_load_lds_dwordx4 v132, s[38:39]
	s_add_i32 m0, s53, 0x400
	s_nop 0
	global_load_lds_dwordx4 v133, s[38:39]
	s_add_u32 s48, s34, 0x18000
	s_addc_u32 s49, s35, 0
	s_add_u32 s50, s38, 0xc0000
	s_addc_u32 s51, s39, 0
	s_add_i32 m0, s52, 0x4000
	s_nop 0
	global_load_lds_dwordx4 v130, s[48:49]
	s_add_i32 m0, s52, 0x4400
	s_nop 0
	global_load_lds_dwordx4 v131, s[48:49]
	s_add_i32 m0, s53, 0x4000
	s_nop 0
	global_load_lds_dwordx4 v132, s[50:51]
	s_add_i32 m0, s53, 0x4400
	s_nop 0
	global_load_lds_dwordx4 v133, s[50:51]
	s_add_u32 s48, s48, 0x18000
	s_addc_u32 s49, s49, 0
	s_add_u32 s50, s50, 0xc0000
	s_addc_u32 s51, s51, 0
	v_lshlrev_b32_e32 v52, 1, v8
	v_add_u32_e32 v54, 0xc000, v52
	v_and_b32_e32 v20, 0xfffff0, v16
	v_lshlrev_b32_e32 v21, 1, v16
	v_lshrrev_b32_e32 v22, 1, v16
	v_and_b32_e32 v23, 3, v16
	v_add_u32_e32 v24, 32, v16
	v_and_or_b32 v20, v21, 8, v20
	v_and_or_b32 v21, v22, 4, v23
	v_and_b32_e32 v22, 0xfffff0, v24
	v_lshlrev_b32_e32 v23, 1, v24
	v_bfe_u32 v17, v17, 5, 2
	v_lshrrev_b32_e32 v20, 1, v20
	v_and_or_b32 v22, v23, 8, v22
	v_lshlrev_b32_e32 v18, 1, v18
	v_or_b32_e32 v20, v20, v17
	v_lshrrev_b32_e32 v22, 1, v22
	v_lshlrev_b32_e32 v21, 6, v21
	v_and_b32_e32 v25, 48, v18
	v_lshlrev_b32_e32 v20, 9, v20
	v_or_b32_e32 v17, v22, v17
	v_or3_b32 v20, v20, v21, v25
	v_lshlrev_b32_e32 v17, 9, v17
	v_or3_b32 v17, v17, v21, v25
	v_add_u32_e32 v205, 0, v20
	v_and_b32_e32 v19, 0x70, v142
	v_lshlrev_b32_e32 v16, 8, v16
	v_add_u32_e32 v206, 0, v17
	s_waitcnt vmcnt(0)
	v_bitop3_b32 v16, v18, v16, v19 bitop3:0xde
	v_lshlrev_b32_e32 v0, 8, v24
	v_bitop3_b32 v0, v18, v0, v19 bitop3:0xde
	v_add_u32_e32 v207, 0, v16
	v_add_u32_e32 v208, 0, v0
	v_lshlrev_b32_e32 v0, 4, v197
	v_lshlrev_b32_e32 v8, 8, v197
	v_and_b32_e32 v9, 0x70, v0
	v_bitop3_b32 v0, v96, v8, v9 bitop3:0xde
	v_add_u32_e32 v209, 0, v0
	s_waitcnt lgkmcnt(0)
	s_barrier
; #define SWRITE(b, i) do { *(LAS bf16x8*)(V_lds + (b) * SHM_V + vst0) = sr_[i].vs0;          \
;     *(LAS bf16x8*)(V_lds + (b) * SHM_V + vst1) = sr_[i].vs1; int kc = sc * 2;               \
;     *(LAS bf16x8*)(K_lds + (b) * SHM_K + KSWZ(sr, kc)) = sr_[i].ks0;                       \
;     *(LAS bf16x8*)(K_lds + (b) * SHM_K + KSWZ(32 + sr, kc)) = sr_[i].ks1; } while (0)
; #define SWAIT() asm volatile("s_waitcnt vmcnt(4)" ::: "memory")
; template <bool HALF> __device__ __forceinline__ void qkt(f32x16& p0, f32x16& p1, const char* Ks, const bf16x8* qr, int r32, int hi, int koff) {
;   p0 = f32x16{}; p1 = f32x16{};
;   for (int d0 = 0; d0 < (HALF ? 4 : 8); ++d0) { int cb = (d0 * 16 + hi * 8) * 2 + koff;
;     bf16x8 b0 = *reinterpret_cast<const bf16x8*>(Ks + KSWZ(r32, cb));
;     bf16x8 b1 = *reinterpret_cast<const bf16x8*>(Ks + KSWZ(32 + r32, cb));
;     p0 = __builtin_amdgcn_mfma_f32_32x32x16_bf16(b0, qr[d0], p0, 0, 0, 0);
;     p1 = __builtin_amdgcn_mfma_f32_32x32x16_bf16(b1, qr[d0], p1, 0, 0, 0); }
; template <bool HALF> __device__ __forceinline__ void dense_body(const bf16_t* __restrict__ Qb, const bf16_t* __restrict__ Kh, const bf16_t* __restrict__ Vh, ...
;     ...
;   qkt<HALF>(pA0, pA1, Kl0, qr, r32, hi, koff); partialSM(pA0, pA1, m_reg, mnA, alA);
;   SLOAD(SO, KVBLK); if (2 < NT) SLOAD(SE, 2 * KVBLK);
;   SWAIT(); SWRITE(1, SO); __syncthreads();
	ds_read_b128 v[0:3], v209 offset:32768
	ds_read_b128 v[4:7], v209 offset:40960
	s_waitcnt lgkmcnt(1)
	v_mfma_f32_32x32x16_bf16 v[16:31], v[0:3], v[118:121], 0
	v_or_b32_e32 v0, 32, v96
	v_bitop3_b32 v0, v0, v8, v9 bitop3:0xde
	v_add_u32_e32 v221, 0, v0
	v_and_b32_e32 v76, 63, v142
	v_and_b32_e32 v10, 0x3fffffc0, v142
	s_add_i32 s46, 0, 0x10000
	v_lshl_add_u32 v200, v10, 2, s46
	s_waitcnt lgkmcnt(0)
	v_mfma_f32_32x32x16_bf16 v[32:47], v[4:7], v[118:121], 0
	ds_read_b128 v[0:3], v221 offset:32768
	ds_read_b128 v[4:7], v221 offset:40960
	v_lshlrev_b32_e32 v10, 3, v76
	s_add_u32 s6, s34, 0x18000
	s_addc_u32 s7, s35, 0
	s_add_u32 s16, s38, 0xc0000
	s_addc_u32 s17, s39, 0
	s_mov_b32 s64, s65
	s_waitcnt lgkmcnt(1)
	v_mfma_f32_32x32x16_bf16 v[16:31], v[0:3], v[126:129], v[16:31]
	v_or_b32_e32 v0, 64, v96
	v_bitop3_b32 v0, v0, v8, v9 bitop3:0xde
	v_add_u32_e32 v222, 0, v0
	s_mov_b32 s66, s65
	s_mov_b32 s67, s65
	s_mov_b32 s68, s65
	s_mov_b32 s69, s65
	s_waitcnt lgkmcnt(0)
	v_mfma_f32_32x32x16_bf16 v[32:47], v[4:7], v[126:129], v[32:47]
	ds_read_b128 v[0:3], v222 offset:32768
	ds_read_b128 v[4:7], v222 offset:40960
	s_mov_b32 s70, s65
	s_mov_b32 s71, s65
	s_mov_b32 s72, s65
	s_mov_b32 s73, s65
	s_mov_b32 s74, s65
	s_mov_b32 s75, s65
	s_waitcnt lgkmcnt(1)
	v_mfma_f32_32x32x16_bf16 v[16:31], v[0:3], v[122:125], v[16:31]
	v_or_b32_e32 v0, 0x60, v96
	v_bitop3_b32 v0, v0, v8, v9 bitop3:0xde
	v_add_u32_e32 v210, 0, v0
	s_mov_b32 s76, s65
	s_mov_b32 s77, s65
	s_mov_b32 s78, s65
	s_mov_b32 s79, s65
	s_waitcnt lgkmcnt(0)
	v_mfma_f32_32x32x16_bf16 v[32:47], v[4:7], v[122:125], v[32:47]
	ds_read_b128 v[0:3], v210 offset:32768
	ds_read_b128 v[4:7], v210 offset:40960
	v_mov_b32_e32 v51, v97
	v_mov_b32_e32 v49, v97
	v_mov_b32_e32 v53, v97
	v_mov_b32_e32 v55, v97
	v_lshl_add_u64 v[180:181], s[22:23], 0, v[50:51]
	v_lshl_add_u64 v[182:183], s[22:23], 0, v[48:49]
	s_waitcnt lgkmcnt(1)
	v_mfma_f32_32x32x16_bf16 v[16:31], v[0:3], v[114:117], v[16:31]
	v_or_b32_e32 v0, 0x80, v96
	v_bitop3_b32 v0, v0, v8, v9 bitop3:0xde
	v_add_u32_e32 v211, 0, v0
	ds_read_b128 v[0:3], v211 offset:32768
	v_lshl_add_u64 v[184:185], s[20:21], 0, v[52:53]
	v_lshl_add_u64 v[186:187], s[20:21], 0, v[54:55]
	s_mov_b32 s2, 4
	s_waitcnt lgkmcnt(1)
	v_mfma_f32_32x32x16_bf16 v[32:47], v[4:7], v[114:117], v[32:47]
	ds_read_b128 v[4:7], v211 offset:40960
	v_cmp_gt_u32_e64 s[40:41], 32, v76
	v_lshl_add_u32 v201, v197, 2, v200
	v_mov_b32_e32 v202, 0
	s_waitcnt lgkmcnt(1)
	v_mfma_f32_32x32x16_bf16 v[16:31], v[0:3], v[110:113], v[16:31]
	v_lshlrev_b32_e32 v0, 4, v76
	v_and_b32_e32 v0, 0xc0, v0
	v_and_or_b32 v11, v10, 24, v0
	v_or_b32_e32 v0, 0xa0, v96
	v_bitop3_b32 v0, v0, v8, v9 bitop3:0xde
	v_add_u32_e32 v223, 0, v0
	v_and_b32_e32 v10, 0x100, v10
	s_waitcnt lgkmcnt(0)
	v_mfma_f32_32x32x16_bf16 v[32:47], v[4:7], v[110:113], v[32:47]
	ds_read_b128 v[0:3], v223 offset:32768
	ds_read_b128 v[4:7], v223 offset:40960
	s_add_u32 s6, s34, 0x30000
	s_addc_u32 s7, s35, 0
	s_waitcnt lgkmcnt(1)
	v_mfma_f32_32x32x16_bf16 v[16:31], v[0:3], v[106:109], v[16:31]
	v_lshlrev_b32_e32 v0, 1, v76
	v_and_b32_e32 v12, 32, v0
	v_or_b32_e32 v0, 0xc0, v96
	v_bitop3_b32 v0, v0, v8, v9 bitop3:0xde
	v_add_u32_e32 v225, 0, v0
	ds_read_b128 v[0:3], v225 offset:32768
	v_or3_b32 v77, v11, v12, v10
	s_waitcnt lgkmcnt(1)
	v_mfma_f32_32x32x16_bf16 v[32:47], v[4:7], v[106:109], v[32:47]
	ds_read_b128 v[4:7], v225 offset:40960
	v_add_u32_e32 v204, 0, v77
	s_waitcnt lgkmcnt(1)
	v_mfma_f32_32x32x16_bf16 v[16:31], v[0:3], v[102:105], v[16:31]
	v_or_b32_e32 v0, 0xe0, v96
	v_bitop3_b32 v0, v0, v8, v9 bitop3:0xde
	v_add_u32_e32 v224, 0, v0
	ds_read_b128 v[0:3], v224 offset:32768
	ds_read_b128 v[72:75], v224 offset:40960
	s_add_u32 s6, s38, 0x180000
	s_addc_u32 s7, s39, 0
	s_waitcnt lgkmcnt(2)
	v_mfma_f32_32x32x16_bf16 v[32:47], v[4:7], v[102:105], v[32:47]
	s_waitcnt lgkmcnt(1)
	v_mfma_f32_32x32x16_bf16 v[16:31], v[0:3], v[98:101], v[16:31]
	v_mov_b64_e32 v[0:1], s[64:65]
	v_mov_b64_e32 v[14:15], s[78:79]
	v_mov_b64_e32 v[2:3], s[66:67]
	v_mov_b64_e32 v[4:5], s[68:69]
	v_mov_b64_e32 v[6:7], s[70:71]
	v_mov_b64_e32 v[8:9], s[72:73]
	v_mov_b64_e32 v[10:11], s[74:75]
	s_waitcnt lgkmcnt(0)
	v_mfma_f32_32x32x16_bf16 v[32:47], v[72:75], v[98:101], v[32:47]
	s_nop 2
	v_max_f32_e32 v72, v17, v17
	v_max_f32_e32 v73, v16, v16
	v_max_f32_e32 v72, v73, v72
	v_max3_f32 v72, v72, v18, v19
	v_max3_f32 v72, v72, v20, v21
	v_max3_f32 v72, v72, v22, v23
	v_max3_f32 v72, v72, v24, v25
	v_max3_f32 v72, v72, v26, v27
	v_max3_f32 v72, v72, v28, v29
	v_max3_f32 v72, v72, v30, v31
	v_max3_f32 v72, v72, v32, v33
	v_max3_f32 v72, v72, v34, v35
	v_max3_f32 v72, v72, v36, v37
	v_max3_f32 v72, v72, v38, v39
	v_max3_f32 v72, v72, v40, v41
	v_max3_f32 v72, v72, v42, v43
	v_max3_f32 v72, v72, v44, v45
	v_max3_f32 v72, v72, v46, v47
	v_mov_b32_e32 v73, v72
	s_nop 1
	v_permlane32_swap_b32_e32 v72, v73
	v_max_f32_e32 v73, v73, v73
	v_max_f32_e32 v72, v72, v72
	v_max_f32_e32 v72, v72, v73
	v_add_f32_e32 v73, 0x7149f2ca, v72
	v_cmp_ge_f32_e32 vcc, s87, v73
	s_cmp_eq_u64 vcc, exec
	v_max_f32_e32 v56, 0xf149f2ca, v72
	s_cselect_b64 vcc, -1, 0
	v_cndmask_b32_e32 v170, v56, v217, vcc
	v_sub_f32_e32 v57, 0xf149f2ca, v56
	v_mul_f32_e32 v56, 0xbe0293ee, v170
	v_fmamk_f32 v16, v16, 0x3e0293ee, v56
	v_exp_f32_e32 v163, v16
	v_fmamk_f32 v16, v17, 0x3e0293ee, v56
	v_exp_f32_e32 v177, v16
	v_fmamk_f32 v16, v18, 0x3e0293ee, v56
	v_exp_f32_e32 v164, v16
	v_fmamk_f32 v16, v19, 0x3e0293ee, v56
	v_exp_f32_e32 v188, v16
	v_fmamk_f32 v16, v20, 0x3e0293ee, v56
	v_exp_f32_e32 v176, v16
	v_fmamk_f32 v16, v21, 0x3e0293ee, v56
	v_exp_f32_e32 v189, v16
	v_fmamk_f32 v16, v22, 0x3e0293ee, v56
; #define SBAR() __builtin_amdgcn_sched_barrier(0)
; #define SWRITE(b, i) do { *(LAS bf16x8*)(V_lds + (b) * SHM_V + vst0) = sr_[i].vs0;          \
;     *(LAS bf16x8*)(V_lds + (b) * SHM_V + vst1) = sr_[i].vs1; int kc = sc * 2;               \
;     *(LAS bf16x8*)(K_lds + (b) * SHM_K + KSWZ(sr, kc)) = sr_[i].ks0;                       \
;     *(LAS bf16x8*)(K_lds + (b) * SHM_K + KSWZ(32 + sr, kc)) = sr_[i].ks1; } while (0)
; #define SWAIT() asm volatile("s_waitcnt vmcnt(4)" ::: "memory")
; __device__ __forceinline__ void partialSM(f32x16& p0, f32x16& p1, float& m_reg, float& mn, float& alpha) {
;     ...
;   else { mn = fmaxf(m_reg, pmax); alpha = __builtin_amdgcn_exp2f((m_reg - mn) * C); m_reg = mn; }
;   float mnC = -mn * C;
;   for (int r = 0; r < 16; ++r) p0[r] = fmaf(p0[r], C, mnC); for (int r = 0; r < 16; ++r) p1[r] = fmaf(p1[r], C, mnC);
;   for (int r = 0; r < 16; ++r) p0[r] = __builtin_amdgcn_exp2f(p0[r]);
; }
; __device__ __forceinline__ void finishSM(f32x16& p0, f32x16& p1, float alpha, float& l_reg, bf16x8& pa0, bf16x8& pa1, bf16x8& pa2, bf16x8& pa3) {
;   for (int r = 0; r < 16; ++r) p1[r] = __builtin_amdgcn_exp2f(p1[r]);
;   float ps = 0; for (int r = 0; r < 16; ++r) ps += p0[r]; for (int r = 0; r < 16; ++r) ps += p1[r];
;   { auto rr = __builtin_amdgcn_permlane32_swap(__float_as_uint(ps), __float_as_uint(ps), false, false);
;     ps = __uint_as_float(rr[0]) + __uint_as_float(rr[1]); }
;   l_reg = l_reg * alpha + ps;
; template <bool HALF> __device__ __forceinline__ void dense_body(const bf16_t* __restrict__ Qb, const bf16_t* __restrict__ Kh, const bf16_t* __restrict__ Vh, ...
;     ...
;   qkt<HALF>(pA0, pA1, Kl0, qr, r32, hi, koff); partialSM(pA0, pA1, m_reg, mnA, alA);
;   SLOAD(SO, KVBLK); if (2 < NT) SLOAD(SE, 2 * KVBLK);
;   SWAIT(); SWRITE(1, SO); __syncthreads();
;   for (int j = 1; j + 1 < NT; j += 2) {
;     SBAR(); qkt<HALF>(pB0, pB1, Kl1, qr, r32, hi, koff);
;     finishSM(pA0, pA1, alA, l_reg, pa0, pa1, pa2, pa3); SBAR();
	v_exp_f32_e32 v165, v16
	v_fmamk_f32 v16, v23, 0x3e0293ee, v56
	v_exp_f32_e32 v175, v16
	v_fmamk_f32 v16, v24, 0x3e0293ee, v56
	v_mul_f32_e32 v57, 0x3e0293ee, v57
	v_exp_f32_e32 v166, v16
	v_fmamk_f32 v16, v25, 0x3e0293ee, v56
	v_exp_f32_e32 v57, v57
	v_exp_f32_e32 v173, v16
	v_fmamk_f32 v16, v26, 0x3e0293ee, v56
	v_exp_f32_e32 v167, v16
	v_fmamk_f32 v16, v27, 0x3e0293ee, v56
	v_exp_f32_e32 v174, v16
	v_fmamk_f32 v16, v28, 0x3e0293ee, v56
	v_exp_f32_e32 v168, v16
	v_fmamk_f32 v16, v29, 0x3e0293ee, v56
	v_pk_fma_f32 v[146:147], v[46:47], s[10:11], v[56:57] op_sel_hi:[1,0,0]
	v_pk_fma_f32 v[152:153], v[44:45], s[10:11], v[56:57] op_sel_hi:[1,0,0]
	v_pk_fma_f32 v[156:157], v[42:43], s[10:11], v[56:57] op_sel_hi:[1,0,0]
	v_pk_fma_f32 v[148:149], v[40:41], s[10:11], v[56:57] op_sel_hi:[1,0,0]
	v_pk_fma_f32 v[150:151], v[38:39], s[10:11], v[56:57] op_sel_hi:[1,0,0]
	v_pk_fma_f32 v[154:155], v[36:37], s[10:11], v[56:57] op_sel_hi:[1,0,0]
	v_pk_fma_f32 v[158:159], v[34:35], s[10:11], v[56:57] op_sel_hi:[1,0,0]
	v_pk_fma_f32 v[160:161], v[32:33], s[10:11], v[56:57] op_sel_hi:[1,0,0]
	v_exp_f32_e32 v171, v16
	v_fmamk_f32 v16, v30, 0x3e0293ee, v56
	v_fmac_f32_e32 v56, 0x3e0293ee, v31
	v_exp_f32_e32 v169, v16
	v_exp_f32_e32 v172, v56
	v_mov_b64_e32 v[12:13], s[76:77]
	v_cndmask_b32_e64 v226, v57, 1.0, vcc
	s_add_i32 s34, 0, 0x4000
	v_mov_b64_e32 v[62:63], v[14:15]
	v_mov_b64_e32 v[46:47], v[14:15]
	v_mov_b64_e32 v[30:31], v[14:15]
	v_add_u32_e32 v203, s34, v77
	v_mov_b64_e32 v[60:61], v[12:13]
	v_mov_b64_e32 v[58:59], v[10:11]
	v_mov_b64_e32 v[56:57], v[8:9]
	v_mov_b64_e32 v[54:55], v[6:7]
	v_mov_b64_e32 v[52:53], v[4:5]
	v_mov_b64_e32 v[50:51], v[2:3]
	v_mov_b64_e32 v[48:49], v[0:1]
	v_mov_b64_e32 v[44:45], v[12:13]
	v_mov_b64_e32 v[42:43], v[10:11]
	v_mov_b64_e32 v[40:41], v[8:9]
	v_mov_b64_e32 v[38:39], v[6:7]
	v_mov_b64_e32 v[36:37], v[4:5]
	v_mov_b64_e32 v[34:35], v[2:3]
	v_mov_b64_e32 v[32:33], v[0:1]
	v_mov_b64_e32 v[28:29], v[12:13]
	v_mov_b64_e32 v[26:27], v[10:11]
	v_mov_b64_e32 v[24:25], v[8:9]
	v_mov_b64_e32 v[22:23], v[6:7]
	v_mov_b64_e32 v[20:21], v[4:5]
	v_mov_b64_e32 v[18:19], v[2:3]
	v_mov_b64_e32 v[16:17], v[0:1]
	s_waitcnt lgkmcnt(0)
	s_barrier
	s_add_i32 m0, s52, 0x0
	s_nop 0
	global_load_lds_dwordx4 v130, s[48:49]
	s_add_i32 m0, s52, 0x400
	s_nop 0
	global_load_lds_dwordx4 v131, s[48:49]
	s_add_u32 s48, s48, 0x18000
	s_addc_u32 s49, s49, 0
.LBB0_425:
	ds_read_b128 v[64:67], v209 offset:49152
	ds_read_b128 v[68:71], v209 offset:57344
	ds_read_b128 v[190:193], v221 offset:49152
	ds_read_b128 v[228:231], v221 offset:57344
	v_add_f32_e32 v162, 0, v163
	v_add_f32_e32 v162, v177, v162
	s_waitcnt lgkmcnt(3)
	v_mfma_f32_32x32x16_bf16 v[80:95], v[64:67], v[118:121], 0
	v_add_f32_e32 v162, v164, v162
	v_add_f32_e32 v162, v188, v162
	v_add_f32_e32 v162, v176, v162
	v_add_f32_e32 v162, v189, v162
	v_add_f32_e32 v162, v165, v162
	v_add_f32_e32 v162, v175, v162
	v_add_f32_e32 v162, v166, v162
	s_waitcnt lgkmcnt(2)
	v_mfma_f32_32x32x16_bf16 v[64:79], v[68:71], v[118:121], 0
	v_add_f32_e32 v162, v173, v162
	v_add_f32_e32 v162, v167, v162
	v_add_f32_e32 v162, v174, v162
	v_exp_f32_e32 v160, v160
	v_add_f32_e32 v162, v168, v162
	v_exp_f32_e32 v161, v161
	v_add_f32_e32 v162, v171, v162
	s_waitcnt lgkmcnt(1)
	v_mfma_f32_32x32x16_bf16 v[80:95], v[190:193], v[126:129], v[80:95]
	v_exp_f32_e32 v158, v158
	v_add_f32_e32 v162, v169, v162
	v_exp_f32_e32 v159, v159
	v_add_f32_e32 v162, v172, v162
	v_exp_f32_e32 v154, v154
	v_add_f32_e32 v162, v160, v162
	v_exp_f32_e32 v155, v155
	s_waitcnt lgkmcnt(0)
	v_mfma_f32_32x32x16_bf16 v[64:79], v[228:231], v[126:129], v[64:79]
	ds_read_b128 v[190:193], v222 offset:49152
	ds_read_b128 v[228:231], v222 offset:57344
	v_add_f32_e32 v162, v161, v162
	v_exp_f32_e32 v150, v150
	v_add_f32_e32 v162, v158, v162
	v_exp_f32_e32 v151, v151
	v_add_f32_e32 v162, v159, v162
	v_exp_f32_e32 v148, v148
	s_waitcnt lgkmcnt(1)
	v_mfma_f32_32x32x16_bf16 v[80:95], v[190:193], v[122:125], v[80:95]
	v_add_f32_e32 v162, v154, v162
	v_exp_f32_e32 v149, v149
	v_add_f32_e32 v162, v155, v162
	v_exp_f32_e32 v156, v156
	v_add_f32_e32 v162, v150, v162
	v_exp_f32_e32 v157, v157
	v_add_f32_e32 v162, v151, v162
	s_waitcnt lgkmcnt(0)
	v_mfma_f32_32x32x16_bf16 v[64:79], v[228:231], v[122:125], v[64:79]
	ds_read_b128 v[190:193], v210 offset:49152
	ds_read_b128 v[228:231], v210 offset:57344
	v_exp_f32_e32 v152, v152
	v_add_f32_e32 v162, v148, v162
	v_exp_f32_e32 v153, v153
	v_add_f32_e32 v162, v149, v162
	v_exp_f32_e32 v146, v146
	v_add_f32_e32 v162, v156, v162
	s_waitcnt lgkmcnt(1)
	v_mfma_f32_32x32x16_bf16 v[80:95], v[190:193], v[114:117], v[80:95]
	v_exp_f32_e32 v147, v147
	v_add_f32_e32 v162, v157, v162
	v_add_f32_e32 v162, v152, v162
	v_add_f32_e32 v162, v153, v162
	v_add_f32_e32 v162, v146, v162
	v_add_f32_e32 v227, v147, v162
	s_waitcnt lgkmcnt(0)
	v_mfma_f32_32x32x16_bf16 v[64:79], v[228:231], v[114:117], v[64:79]
	ds_read_b128 v[190:193], v211 offset:49152
	ds_read_b128 v[228:231], v211 offset:57344
	s_waitcnt lgkmcnt(1)
	v_mfma_f32_32x32x16_bf16 v[80:95], v[190:193], v[110:113], v[80:95]
	s_waitcnt lgkmcnt(0)
	v_mfma_f32_32x32x16_bf16 v[64:79], v[228:231], v[110:113], v[64:79]
	ds_read_b128 v[190:193], v223 offset:49152
	ds_read_b128 v[228:231], v223 offset:57344
	s_waitcnt lgkmcnt(1)
	v_mfma_f32_32x32x16_bf16 v[80:95], v[190:193], v[106:109], v[80:95]
	s_waitcnt lgkmcnt(0)
	v_mfma_f32_32x32x16_bf16 v[64:79], v[228:231], v[106:109], v[64:79]
	ds_read_b128 v[190:193], v225 offset:49152
	ds_read_b128 v[228:231], v225 offset:57344
	s_waitcnt lgkmcnt(1)
	v_mfma_f32_32x32x16_bf16 v[80:95], v[190:193], v[102:105], v[80:95]
	s_waitcnt lgkmcnt(0)
; #define SBAR() __builtin_amdgcn_sched_barrier(0)
; __device__ __forceinline__ void finishSM(f32x16& p0, f32x16& p1, float alpha, float& l_reg, bf16x8& pa0, bf16x8& pa1, bf16x8& pa2, bf16x8& pa3) {
;     ...
;   PK4(p0, 0, pa0); PK4(p0, 8, pa1); PK4(p1, 0, pa2); PK4(p1, 8, pa3);
; template <int D0> __device__ __forceinline__ void pv_one(f32x16& od, int vb, bf16x8 pa0, bf16x8 pa1, bf16x8 pa2, bf16x8 pa3) {
;   const s16x4 l0 = tr_read<v_rd_off(D0, 0, 0)>(vb), h0 = tr_read<v_rd_off(D0, 0, 1)>(vb), l1 = tr_read<v_rd_off(D0, 1, 0)>(vb), h1 = tr_read<v_rd_off(D0, 1, 1)>(vb);
;   const s16x4 l2 = tr_read<v_rd_off(D0, 2, 0)>(vb), h2 = tr_read<v_rd_off(D0, 2, 1)>(vb), l3 = tr_read<v_rd_off(D0, 3, 0)>(vb), h3 = tr_read<v_rd_off(D0, 3, 1)>(vb);
;   asm volatile("s_waitcnt lgkmcnt(0)" ::: "memory"); SBAR();
;     ...
;   od = __builtin_amdgcn_mfma_f32_32x32x16_bf16(pa0, PK(l0, h0), od, 0, 0, 0);
;   od = __builtin_amdgcn_mfma_f32_32x32x16_bf16(pa1, PK(l1, h1), od, 0, 0, 0);
;   od = __builtin_amdgcn_mfma_f32_32x32x16_bf16(pa2, PK(l2, h2), od, 0, 0, 0);
;   od = __builtin_amdgcn_mfma_f32_32x32x16_bf16(pa3, PK(l3, h3), od, 0, 0, 0);
; template <bool HALF> __device__ __forceinline__ void dense_body(const bf16_t* __restrict__ Qb, const bf16_t* __restrict__ Kh, const bf16_t* __restrict__ Vh, ...
;     ...
;     finishSM(pA0, pA1, alA, l_reg, pa0, pa1, pa2, pa3); SBAR();
;     SLOAD(SO, (j + 2) * KVBLK); SBAR();
;     pv_d0(o, vb0, pa0, pa1, pa2, pa3); partialSM(pB0, pB1, m_reg, mnB, alB);
	v_mfma_f32_32x32x16_bf16 v[64:79], v[228:231], v[102:105], v[64:79]
	ds_read_b128 v[190:193], v224 offset:49152
	ds_read_b128 v[228:231], v224 offset:57344
	v_cvt_pk_bf16_f32 v162, v163, v177
	v_cvt_pk_bf16_f32 v163, v164, v188
	v_cvt_pk_bf16_f32 v164, v176, v189
	v_cvt_pk_bf16_f32 v165, v165, v175
	v_cvt_pk_bf16_f32 v166, v166, v173
	v_cvt_pk_bf16_f32 v167, v167, v174
	s_waitcnt lgkmcnt(1)
	v_mfma_f32_32x32x16_bf16 v[80:95], v[190:193], v[98:101], v[80:95]
	v_permlane32_swap_b32_e32 v162, v164
	v_cvt_pk_bf16_f32 v168, v168, v171
	v_cvt_pk_bf16_f32 v169, v169, v172
	v_cvt_pk_bf16_f32 v172, v160, v161
	v_cvt_pk_bf16_f32 v173, v158, v159
	v_cvt_pk_bf16_f32 v174, v154, v155
	s_waitcnt lgkmcnt(0)
	v_mfma_f32_32x32x16_bf16 v[64:79], v[228:231], v[98:101], v[64:79]
	v_mov_b32_e32 v228, v227
	s_nop 1
	v_permlane32_swap_b32_e32 v227, v228
	v_cvt_pk_bf16_f32 v175, v150, v151
	v_cvt_pk_bf16_f32 v230, v148, v149
	v_cvt_pk_bf16_f32 v231, v156, v157
	v_cvt_pk_bf16_f32 v232, v152, v153
	v_cvt_pk_bf16_f32 v233, v146, v147
	v_permlane32_swap_b32_e32 v163, v165
	v_permlane32_swap_b32_e32 v166, v168
	v_permlane32_swap_b32_e32 v167, v169
	v_permlane32_swap_b32_e32 v172, v174
	v_permlane32_swap_b32_e32 v173, v175
	v_permlane32_swap_b32_e32 v230, v232
	v_permlane32_swap_b32_e32 v231, v233
	ds_read_b64_tr_b16 v[234:235], v204 offset:0
	ds_read_b64_tr_b16 v[236:237], v204 offset:0x800
	ds_read_b64_tr_b16 v[238:239], v204 offset:0x1000
	ds_read_b64_tr_b16 v[240:241], v204 offset:0x1800
	ds_read_b64_tr_b16 v[242:243], v204 offset:0x2000
	ds_read_b64_tr_b16 v[244:245], v204 offset:0x2800
	ds_read_b64_tr_b16 v[246:247], v204 offset:0x3000
	ds_read_b64_tr_b16 v[248:249], v204 offset:0x3800
	s_waitcnt lgkmcnt(0)
	s_nop 0
	v_mfma_f32_32x32x16_bf16 v[0:15], v[162:165], v[234:237], v[0:15]
	ds_read_b64_tr_b16 v[234:235], v204 offset:0x200
	ds_read_b64_tr_b16 v[236:237], v204 offset:0xa00
	v_mfma_f32_32x32x16_bf16 v[0:15], v[166:169], v[238:241], v[0:15]
	ds_read_b64_tr_b16 v[238:239], v204 offset:0x1200
	ds_read_b64_tr_b16 v[240:241], v204 offset:0x1a00
	v_mfma_f32_32x32x16_bf16 v[0:15], v[172:175], v[242:245], v[0:15]
	ds_read_b64_tr_b16 v[242:243], v204 offset:0x2200
	ds_read_b64_tr_b16 v[244:245], v204 offset:0x2a00
	v_mfma_f32_32x32x16_bf16 v[0:15], v[230:233], v[246:249], v[0:15]
	ds_read_b64_tr_b16 v[246:247], v204 offset:0x3200
	ds_read_b64_tr_b16 v[248:249], v204 offset:0x3a00
	s_waitcnt lgkmcnt(0)
	v_mfma_f32_32x32x16_bf16 v[48:63], v[162:165], v[234:237], v[48:63]
	ds_read_b64_tr_b16 v[234:235], v204 offset:0x400
	ds_read_b64_tr_b16 v[236:237], v204 offset:0xc00
	v_mfma_f32_32x32x16_bf16 v[48:63], v[166:169], v[238:241], v[48:63]
	ds_read_b64_tr_b16 v[238:239], v204 offset:0x1400
	ds_read_b64_tr_b16 v[240:241], v204 offset:0x1c00
	v_mfma_f32_32x32x16_bf16 v[48:63], v[172:175], v[242:245], v[48:63]
	ds_read_b64_tr_b16 v[242:243], v204 offset:0x2400
	ds_read_b64_tr_b16 v[244:245], v204 offset:0x2c00
	v_mfma_f32_32x32x16_bf16 v[48:63], v[230:233], v[246:249], v[48:63]
	ds_read_b64_tr_b16 v[246:247], v204 offset:0x3400
	ds_read_b64_tr_b16 v[248:249], v204 offset:0x3c00
	s_waitcnt lgkmcnt(0)
	v_mfma_f32_32x32x16_bf16 v[32:47], v[162:165], v[234:237], v[32:47]
	ds_read_b64_tr_b16 v[234:235], v204 offset:0x600
	ds_read_b64_tr_b16 v[236:237], v204 offset:0xe00
	v_mfma_f32_32x32x16_bf16 v[32:47], v[166:169], v[238:241], v[32:47]
	ds_read_b64_tr_b16 v[238:239], v204 offset:0x1600
	ds_read_b64_tr_b16 v[240:241], v204 offset:0x1e00
	v_mfma_f32_32x32x16_bf16 v[32:47], v[172:175], v[242:245], v[32:47]
	ds_read_b64_tr_b16 v[242:243], v204 offset:0x2600
	ds_read_b64_tr_b16 v[244:245], v204 offset:0x2e00
	v_mfma_f32_32x32x16_bf16 v[32:47], v[230:233], v[246:249], v[32:47]
	ds_read_b64_tr_b16 v[246:247], v204 offset:0x3600
	ds_read_b64_tr_b16 v[248:249], v204 offset:0x3e00
	s_waitcnt lgkmcnt(0)
	v_mfma_f32_32x32x16_bf16 v[16:31], v[162:165], v[234:237], v[16:31]
	v_max_f32_e32 v162, v81, v81
	v_max_f32_e32 v163, v80, v80
	v_max_f32_e32 v162, v163, v162
	v_max3_f32 v162, v162, v82, v83
	v_max3_f32 v162, v162, v84, v85
	v_max3_f32 v162, v162, v86, v87
	v_max3_f32 v162, v162, v88, v89
	v_max3_f32 v162, v162, v90, v91
	v_max3_f32 v162, v162, v92, v93
	v_mfma_f32_32x32x16_bf16 v[16:31], v[166:169], v[238:241], v[16:31]
	v_max3_f32 v162, v162, v94, v95
	v_max3_f32 v162, v162, v64, v65
	v_max3_f32 v162, v162, v66, v67
	v_max3_f32 v162, v162, v68, v69
	v_max3_f32 v162, v162, v70, v71
	v_max3_f32 v162, v162, v72, v73
	v_max3_f32 v162, v162, v74, v75
	v_max3_f32 v162, v162, v76, v77
	v_mfma_f32_32x32x16_bf16 v[16:31], v[172:175], v[242:245], v[16:31]
	v_max3_f32 v162, v162, v78, v79
	v_mov_b32_e32 v163, v162
	s_nop 1
	v_permlane32_swap_b32_e32 v162, v163
	v_max_f32_e32 v163, v163, v163
	v_max_f32_e32 v162, v162, v162
	v_max_f32_e32 v162, v162, v163
	v_sub_f32_e32 v163, v162, v170
	v_cmp_ge_f32_e32 vcc, s87, v163
	v_max_f32_e32 v163, v170, v170
	v_max_f32_e32 v162, v163, v162
	v_mfma_f32_32x32x16_bf16 v[16:31], v[230:233], v[246:249], v[16:31]
	v_sub_f32_e32 v163, v170, v162
	v_mul_f32_e32 v163, 0x3e0293ee, v163
	v_exp_f32_e32 v163, v163
	s_cmp_eq_u64 vcc, exec
	s_cselect_b64 s[42:43], -1, 0
	s_barrier
; #define SWRITE(b, i) do { *(LAS bf16x8*)(V_lds + (b) * SHM_V + vst0) = sr_[i].vs0;          \
;     *(LAS bf16x8*)(V_lds + (b) * SHM_V + vst1) = sr_[i].vs1; int kc = sc * 2;               \
;     *(LAS bf16x8*)(K_lds + (b) * SHM_K + KSWZ(sr, kc)) = sr_[i].ks0;                       \
;     *(LAS bf16x8*)(K_lds + (b) * SHM_K + KSWZ(32 + sr, kc)) = sr_[i].ks1; } while (0)
; #define SWAIT() asm volatile("s_waitcnt vmcnt(4)" ::: "memory")
; #define RESC(a) do { if (__any((a) < 1.f)) { if (hi == 0) al_l[r32] = (a); asm volatile("s_waitcnt lgkmcnt(0)" ::: "memory"); \
;     for (int d = 0; d < 4; ++d) for (int r = 0; r < 16; ++r) o[d][r] *= al_l[crow(r, hi)]; } } while (0)
; template <bool HALF> __device__ __forceinline__ void dense_body(const bf16_t* __restrict__ Qb, const bf16_t* __restrict__ Kh, const bf16_t* __restrict__ Vh, ...
;     ...
;     pv_d0(o, vb0, pa0, pa1, pa2, pa3); partialSM(pB0, pB1, m_reg, mnB, alB);
;     __syncthreads(); SWAIT(); SWRITE(0, SE);
;     RESC(alB); __syncthreads();
	s_waitcnt vmcnt(0)
	s_add_i32 m0, s52, 0x4000
	s_nop 0
	global_load_lds_dwordx4 v130, s[48:49]
	s_add_i32 m0, s52, 0x4400
	s_nop 0
	global_load_lds_dwordx4 v131, s[48:49]
	s_add_i32 m0, s53, 0x0
	s_nop 0
	global_load_lds_dwordx4 v132, s[50:51]
	s_add_i32 m0, s53, 0x400
	s_nop 0
	global_load_lds_dwordx4 v133, s[50:51]
	s_add_u32 s48, s48, 0x18000
	s_addc_u32 s49, s49, 0
	s_add_u32 s50, s50, 0xc0000
	s_addc_u32 s51, s51, 0
	v_cndmask_b32_e64 v229, v163, 1.0, s[42:43]
	v_cmp_gt_f32_e32 vcc, 1.0, v229
	s_cbranch_vccz .LBB0_429
	s_and_saveexec_b64 s[6:7], s[40:41]
	ds_write_b32 v201, v229 offset:128
	s_or_b64 exec, exec, s[6:7]
	s_waitcnt lgkmcnt(0)
	v_add_u32_e32 v163, v200, v96
	ds_read_b128 v[164:167], v163 offset:224
	ds_read_b128 v[172:175], v163 offset:192
	ds_read_b128 v[230:233], v163 offset:160
	ds_read_b128 v[234:237], v163 offset:128
	s_waitcnt lgkmcnt(3)
	v_pk_mul_f32 v[12:13], v[12:13], v[164:165]
	s_waitcnt lgkmcnt(2)
	v_pk_mul_f32 v[8:9], v[8:9], v[172:173]
	s_waitcnt lgkmcnt(1)
	v_pk_mul_f32 v[4:5], v[4:5], v[230:231]
	v_pk_mul_f32 v[14:15], v[14:15], v[166:167]
	v_pk_mul_f32 v[10:11], v[10:11], v[174:175]
	v_pk_mul_f32 v[6:7], v[6:7], v[232:233]
	s_waitcnt lgkmcnt(0)
	v_pk_mul_f32 v[2:3], v[2:3], v[236:237]
	v_pk_mul_f32 v[0:1], v[0:1], v[234:235]
	v_pk_mul_f32 v[60:61], v[60:61], v[164:165]
	v_pk_mul_f32 v[56:57], v[56:57], v[172:173]
	v_pk_mul_f32 v[52:53], v[52:53], v[230:231]
	v_pk_mul_f32 v[62:63], v[62:63], v[166:167]
	v_pk_mul_f32 v[58:59], v[58:59], v[174:175]
	v_pk_mul_f32 v[54:55], v[54:55], v[232:233]
	v_pk_mul_f32 v[50:51], v[50:51], v[236:237]
	v_pk_mul_f32 v[48:49], v[48:49], v[234:235]
	v_pk_mul_f32 v[44:45], v[44:45], v[164:165]
	v_pk_mul_f32 v[40:41], v[40:41], v[172:173]
	v_pk_mul_f32 v[36:37], v[36:37], v[230:231]
	v_pk_mul_f32 v[46:47], v[46:47], v[166:167]
	v_pk_mul_f32 v[42:43], v[42:43], v[174:175]
	v_pk_mul_f32 v[38:39], v[38:39], v[232:233]
	v_pk_mul_f32 v[34:35], v[34:35], v[236:237]
	v_pk_mul_f32 v[32:33], v[32:33], v[234:235]
	v_pk_mul_f32 v[28:29], v[28:29], v[164:165]
	v_pk_mul_f32 v[24:25], v[24:25], v[172:173]
	v_pk_mul_f32 v[20:21], v[20:21], v[230:231]
	v_pk_mul_f32 v[30:31], v[30:31], v[166:167]
	v_pk_mul_f32 v[26:27], v[26:27], v[174:175]
	v_pk_mul_f32 v[22:23], v[22:23], v[232:233]
	v_pk_mul_f32 v[18:19], v[18:19], v[236:237]
	v_pk_mul_f32 v[16:17], v[16:17], v[234:235]

; #define SBAR() __builtin_amdgcn_sched_barrier(0)
; #define SWRITE(b, i) do { *(LAS bf16x8*)(V_lds + (b) * SHM_V + vst0) = sr_[i].vs0;          \
;     *(LAS bf16x8*)(V_lds + (b) * SHM_V + vst1) = sr_[i].vs1; int kc = sc * 2;               \
;     *(LAS bf16x8*)(K_lds + (b) * SHM_K + KSWZ(sr, kc)) = sr_[i].ks0;                       \
;     *(LAS bf16x8*)(K_lds + (b) * SHM_K + KSWZ(32 + sr, kc)) = sr_[i].ks1; } while (0)
; #define SWAIT() asm volatile("s_waitcnt vmcnt(4)" ::: "memory")
; #define RESC(a) do { if (__any((a) < 1.f)) { if (hi == 0) al_l[r32] = (a); asm volatile("s_waitcnt lgkmcnt(0)" ::: "memory"); \
;     for (int d = 0; d < 4; ++d) for (int r = 0; r < 16; ++r) o[d][r] *= al_l[crow(r, hi)]; } } while (0)
; __device__ __forceinline__ void partialSM(f32x16& p0, f32x16& p1, float& m_reg, float& mn, float& alpha) {
;   constexpr float C = SCALE * 1.4426950408889634f;
;   float pmax = p0[0]; for (int r = 1; r < 16; ++r) pmax = fmaxf(pmax, p0[r]); for (int r = 0; r < 16; ++r) pmax = fmaxf(pmax, p1[r]);
;   { auto rr = __builtin_amdgcn_permlane32_swap(__float_as_uint(pmax), __float_as_uint(pmax), false, false);
;     pmax = fmaxf(__uint_as_float(rr[0]), __uint_as_float(rr[1])); }
;   if (__builtin_expect(__all(pmax - m_reg <= THR / SCALE), 1)) { mn = m_reg; alpha = 1.f; }
;   else { mn = fmaxf(m_reg, pmax); alpha = __builtin_amdgcn_exp2f((m_reg - mn) * C); m_reg = mn; }
; template <bool HALF> __device__ __forceinline__ void dense_body(const bf16_t* __restrict__ Qb, const bf16_t* __restrict__ Kh, const bf16_t* __restrict__ Vh, ...
;     ...
;     if (j + 3 < NT) SLOAD(SE, (j + 3) * KVBLK); SBAR();
;     pv_d0(o, vb0 + (int)SHM_V, pa0, pa1, pa2, pa3); partialSM(pA0, pA1, m_reg, mnA, alA);
;     __syncthreads(); SWAIT(); SWRITE(1, SO);
;     RESC(alA); __syncthreads();
.LBB0_431:
	ds_read_b64_tr_b16 v[188:189], v203 offset:0
	ds_read_b64_tr_b16 v[190:191], v203 offset:0x800
	ds_read_b64_tr_b16 v[192:193], v203 offset:0x1000
	ds_read_b64_tr_b16 v[194:195], v203 offset:0x1800
	ds_read_b64_tr_b16 v[212:213], v203 offset:0x2000
	ds_read_b64_tr_b16 v[214:215], v203 offset:0x2800
	ds_read_b64_tr_b16 v[234:235], v203 offset:0x3000
	ds_read_b64_tr_b16 v[236:237], v203 offset:0x3800
	s_waitcnt lgkmcnt(0)
	s_nop 0
	v_mfma_f32_32x32x16_bf16 v[0:15], v[162:165], v[188:191], v[0:15]
	ds_read_b64_tr_b16 v[188:189], v203 offset:0x200
	ds_read_b64_tr_b16 v[190:191], v203 offset:0xa00
	v_mfma_f32_32x32x16_bf16 v[0:15], v[166:169], v[192:195], v[0:15]
	ds_read_b64_tr_b16 v[192:193], v203 offset:0x1200
	ds_read_b64_tr_b16 v[194:195], v203 offset:0x1a00
	v_mfma_f32_32x32x16_bf16 v[0:15], v[170:173], v[212:215], v[0:15]
	ds_read_b64_tr_b16 v[212:213], v203 offset:0x2200
	ds_read_b64_tr_b16 v[214:215], v203 offset:0x2a00
	v_mfma_f32_32x32x16_bf16 v[0:15], v[174:177], v[234:237], v[0:15]
	ds_read_b64_tr_b16 v[234:235], v203 offset:0x3200
	ds_read_b64_tr_b16 v[236:237], v203 offset:0x3a00
	s_waitcnt lgkmcnt(0)
	v_mfma_f32_32x32x16_bf16 v[48:63], v[162:165], v[188:191], v[48:63]
	ds_read_b64_tr_b16 v[188:189], v203 offset:0x400
	ds_read_b64_tr_b16 v[190:191], v203 offset:0xc00
	v_mfma_f32_32x32x16_bf16 v[48:63], v[166:169], v[192:195], v[48:63]
	ds_read_b64_tr_b16 v[192:193], v203 offset:0x1400
	ds_read_b64_tr_b16 v[194:195], v203 offset:0x1c00
	v_mfma_f32_32x32x16_bf16 v[48:63], v[170:173], v[212:215], v[48:63]
	ds_read_b64_tr_b16 v[212:213], v203 offset:0x2400
	ds_read_b64_tr_b16 v[214:215], v203 offset:0x2c00
	v_mfma_f32_32x32x16_bf16 v[48:63], v[174:177], v[234:237], v[48:63]
	ds_read_b64_tr_b16 v[234:235], v203 offset:0x3400
	ds_read_b64_tr_b16 v[236:237], v203 offset:0x3c00
	s_waitcnt lgkmcnt(0)
	v_mfma_f32_32x32x16_bf16 v[32:47], v[162:165], v[188:191], v[32:47]
	ds_read_b64_tr_b16 v[188:189], v203 offset:0x600
	ds_read_b64_tr_b16 v[190:191], v203 offset:0xe00
	v_mfma_f32_32x32x16_bf16 v[32:47], v[166:169], v[192:195], v[32:47]
	ds_read_b64_tr_b16 v[192:193], v203 offset:0x1600
	ds_read_b64_tr_b16 v[194:195], v203 offset:0x1e00
	v_mfma_f32_32x32x16_bf16 v[32:47], v[170:173], v[212:215], v[32:47]
	ds_read_b64_tr_b16 v[212:213], v203 offset:0x2600
	ds_read_b64_tr_b16 v[214:215], v203 offset:0x2e00
	v_mfma_f32_32x32x16_bf16 v[32:47], v[174:177], v[234:237], v[32:47]
	ds_read_b64_tr_b16 v[234:235], v203 offset:0x3600
	ds_read_b64_tr_b16 v[236:237], v203 offset:0x3e00
	s_waitcnt lgkmcnt(0)
	v_mfma_f32_32x32x16_bf16 v[16:31], v[162:165], v[188:191], v[16:31]
	v_max_f32_e32 v162, v81, v81
	v_max_f32_e32 v163, v80, v80
	v_max_f32_e32 v162, v163, v162
	v_max3_f32 v162, v162, v82, v83
	v_max3_f32 v162, v162, v84, v85
	v_max3_f32 v162, v162, v86, v87
	v_max3_f32 v162, v162, v88, v89
	v_max3_f32 v162, v162, v90, v91
	v_max3_f32 v162, v162, v92, v93
	v_mfma_f32_32x32x16_bf16 v[16:31], v[166:169], v[192:195], v[16:31]
	v_max3_f32 v162, v162, v94, v95
	v_max3_f32 v162, v162, v64, v65
	v_max3_f32 v162, v162, v66, v67
	v_max3_f32 v162, v162, v68, v69
	v_max3_f32 v162, v162, v70, v71
	v_max3_f32 v162, v162, v72, v73
	v_max3_f32 v162, v162, v74, v75
	v_max3_f32 v162, v162, v76, v77
	v_mfma_f32_32x32x16_bf16 v[16:31], v[170:173], v[212:215], v[16:31]
	v_max3_f32 v162, v162, v78, v79
	v_mov_b32_e32 v163, v162
	s_nop 1
	v_permlane32_swap_b32_e32 v162, v163
	v_max_f32_e32 v163, v163, v163
	v_max_f32_e32 v162, v162, v162
	v_max_f32_e32 v162, v162, v163
	v_sub_f32_e32 v163, v162, v230
	v_cmp_ge_f32_e32 vcc, s87, v163
	v_max_f32_e32 v163, v230, v230
	v_max_f32_e32 v163, v163, v162
	v_mfma_f32_32x32x16_bf16 v[16:31], v[174:177], v[234:237], v[16:31]
	v_sub_f32_e32 v162, v230, v163
	v_mul_f32_e32 v162, 0x3e0293ee, v162
	v_exp_f32_e32 v162, v162
	s_cmp_eq_u64 vcc, exec
	s_cselect_b64 s[42:43], -1, 0
	s_barrier
	s_waitcnt vmcnt(0)
	s_add_i32 m0, s52, 0x0
	s_nop 0
	global_load_lds_dwordx4 v130, s[48:49]
	s_add_i32 m0, s52, 0x400
	s_nop 0
	global_load_lds_dwordx4 v131, s[48:49]
	s_add_i32 m0, s53, 0x4000
	s_nop 0
	global_load_lds_dwordx4 v132, s[50:51]
	s_add_i32 m0, s53, 0x4400
	s_nop 0
	global_load_lds_dwordx4 v133, s[50:51]
	s_add_u32 s48, s48, 0x18000
	s_addc_u32 s49, s49, 0
	s_add_u32 s50, s50, 0xc0000
	s_addc_u32 s51, s51, 0
	v_cndmask_b32_e64 v162, v162, 1.0, s[42:43]
	v_cmp_gt_f32_e32 vcc, 1.0, v162
	s_cbranch_vccz .LBB0_435
	s_and_saveexec_b64 s[6:7], s[40:41]
	ds_write_b32 v201, v162 offset:128
	s_or_b64 exec, exec, s[6:7]
	s_waitcnt lgkmcnt(0)
	v_add_u32_e32 v158, v200, v96
	ds_read_b128 v[146:149], v158 offset:224
	ds_read_b128 v[150:153], v158 offset:192
	ds_read_b128 v[154:157], v158 offset:160
	ds_read_b128 v[158:161], v158 offset:128
	s_waitcnt lgkmcnt(3)
	v_pk_mul_f32 v[12:13], v[12:13], v[146:147]
	s_waitcnt lgkmcnt(2)
	v_pk_mul_f32 v[8:9], v[8:9], v[150:151]
	s_waitcnt lgkmcnt(1)
	v_pk_mul_f32 v[4:5], v[4:5], v[154:155]
	v_pk_mul_f32 v[14:15], v[14:15], v[148:149]
	v_pk_mul_f32 v[10:11], v[10:11], v[152:153]
	v_pk_mul_f32 v[6:7], v[6:7], v[156:157]
	s_waitcnt lgkmcnt(0)
	v_pk_mul_f32 v[2:3], v[2:3], v[160:161]
	v_pk_mul_f32 v[0:1], v[0:1], v[158:159]
	v_pk_mul_f32 v[60:61], v[60:61], v[146:147]
	v_pk_mul_f32 v[56:57], v[56:57], v[150:151]
	v_pk_mul_f32 v[52:53], v[52:53], v[154:155]
	v_pk_mul_f32 v[62:63], v[62:63], v[148:149]
	v_pk_mul_f32 v[58:59], v[58:59], v[152:153]
	v_pk_mul_f32 v[54:55], v[54:55], v[156:157]
	v_pk_mul_f32 v[50:51], v[50:51], v[160:161]
	v_pk_mul_f32 v[48:49], v[48:49], v[158:159]
	v_pk_mul_f32 v[44:45], v[44:45], v[146:147]
	v_pk_mul_f32 v[40:41], v[40:41], v[150:151]
	v_pk_mul_f32 v[36:37], v[36:37], v[154:155]
	v_pk_mul_f32 v[46:47], v[46:47], v[148:149]
	v_pk_mul_f32 v[42:43], v[42:43], v[152:153]
	v_pk_mul_f32 v[38:39], v[38:39], v[156:157]
	v_pk_mul_f32 v[34:35], v[34:35], v[160:161]
	v_pk_mul_f32 v[32:33], v[32:33], v[158:159]
	v_pk_mul_f32 v[28:29], v[28:29], v[146:147]
	v_pk_mul_f32 v[24:25], v[24:25], v[150:151]
	v_pk_mul_f32 v[20:21], v[20:21], v[154:155]
	v_pk_mul_f32 v[30:31], v[30:31], v[148:149]
	v_pk_mul_f32 v[26:27], v[26:27], v[152:153]
	v_pk_mul_f32 v[22:23], v[22:23], v[156:157]
	v_pk_mul_f32 v[18:19], v[18:19], v[160:161]
	v_pk_mul_f32 v[16:17], v[16:17], v[158:159]
; #define SBAR() __builtin_amdgcn_sched_barrier(0)
; #define RESC(a) do { if (__any((a) < 1.f)) { if (hi == 0) al_l[r32] = (a); asm volatile("s_waitcnt lgkmcnt(0)" ::: "memory"); \
;     for (int d = 0; d < 4; ++d) for (int r = 0; r < 16; ++r) o[d][r] *= al_l[crow(r, hi)]; } } while (0)
; __device__ __forceinline__ void partialSM(f32x16& p0, f32x16& p1, float& m_reg, float& mn, float& alpha) {
;     ...
;   else { mn = fmaxf(m_reg, pmax); alpha = __builtin_amdgcn_exp2f((m_reg - mn) * C); m_reg = mn; }
;   float mnC = -mn * C;
;   for (int r = 0; r < 16; ++r) p0[r] = fmaf(p0[r], C, mnC); for (int r = 0; r < 16; ++r) p1[r] = fmaf(p1[r], C, mnC);
;   for (int r = 0; r < 16; ++r) p0[r] = __builtin_amdgcn_exp2f(p0[r]);
; }
; __device__ __forceinline__ void finishSM(f32x16& p0, f32x16& p1, float alpha, float& l_reg, bf16x8& pa0, bf16x8& pa1, bf16x8& pa2, bf16x8& pa3) {
;   for (int r = 0; r < 16; ++r) p1[r] = __builtin_amdgcn_exp2f(p1[r]);
;   float ps = 0; for (int r = 0; r < 16; ++r) ps += p0[r]; for (int r = 0; r < 16; ++r) ps += p1[r];
;   { auto rr = __builtin_amdgcn_permlane32_swap(__float_as_uint(ps), __float_as_uint(ps), false, false);
;     ps = __uint_as_float(rr[0]) + __uint_as_float(rr[1]); }
;   l_reg = l_reg * alpha + ps;
; template <bool HALF> __device__ __forceinline__ void dense_body(const bf16_t* __restrict__ Qb, const bf16_t* __restrict__ Kh, const bf16_t* __restrict__ Vh, ...
;     ...
;     RESC(alA); __syncthreads();
;   }
;   SBAR(); qkt<HALF>(pB0, pB1, Kl1, qr, r32, hi, koff);
;   finishSM(pA0, pA1, alA, l_reg, pa0, pa1, pa2, pa3); SBAR();
;   pv_d0(o, vb0, pa0, pa1, pa2, pa3); partialSM(pB0, pB1, m_reg, mnB, alB);
.LBB0_435:
	v_cndmask_b32_e64 v170, v163, v230, s[42:43]
	v_mul_f32_e32 v146, 0xbe0293ee, v170
	v_mov_b32_e32 v147, v146
	v_fmamk_f32 v80, v80, 0x3e0293ee, v146
	v_fmamk_f32 v81, v81, 0x3e0293ee, v146
	v_fmamk_f32 v82, v82, 0x3e0293ee, v146
	v_fmamk_f32 v83, v83, 0x3e0293ee, v146
	v_fmamk_f32 v84, v84, 0x3e0293ee, v146
	v_fmamk_f32 v85, v85, 0x3e0293ee, v146
	v_fmamk_f32 v86, v86, 0x3e0293ee, v146
	v_fmamk_f32 v87, v87, 0x3e0293ee, v146
	v_fmamk_f32 v88, v88, 0x3e0293ee, v146
	v_fmamk_f32 v89, v89, 0x3e0293ee, v146
	v_fmamk_f32 v90, v90, 0x3e0293ee, v146
	v_fmamk_f32 v91, v91, 0x3e0293ee, v146
	v_fmamk_f32 v92, v92, 0x3e0293ee, v146
	v_fmamk_f32 v93, v93, 0x3e0293ee, v146
	v_fmamk_f32 v94, v94, 0x3e0293ee, v146
	v_fmac_f32_e32 v147, 0x3e0293ee, v95
	v_exp_f32_e32 v163, v80
	v_exp_f32_e32 v177, v81
	v_exp_f32_e32 v164, v82
	v_exp_f32_e32 v188, v83
	v_exp_f32_e32 v176, v84
	v_exp_f32_e32 v189, v85
	v_exp_f32_e32 v165, v86
	v_exp_f32_e32 v175, v87
	v_exp_f32_e32 v166, v88
	v_exp_f32_e32 v173, v89
	v_exp_f32_e32 v167, v90
	v_exp_f32_e32 v174, v91
	v_exp_f32_e32 v168, v92
	v_exp_f32_e32 v171, v93
	v_exp_f32_e32 v169, v94
	v_exp_f32_e32 v172, v147
	v_pk_fma_f32 v[160:161], v[64:65], s[10:11], v[146:147] op_sel_hi:[1,0,0]
	v_add_f32_e32 v64, v227, v228
	v_fmac_f32_e32 v64, v226, v202
	v_add_f32_e32 v202, v231, v232
	v_pk_fma_f32 v[158:159], v[66:67], s[10:11], v[146:147] op_sel_hi:[1,0,0]
	v_pk_fma_f32 v[154:155], v[68:69], s[10:11], v[146:147] op_sel_hi:[1,0,0]
	v_pk_fma_f32 v[150:151], v[70:71], s[10:11], v[146:147] op_sel_hi:[1,0,0]
	v_pk_fma_f32 v[148:149], v[72:73], s[10:11], v[146:147] op_sel_hi:[1,0,0]
	v_pk_fma_f32 v[156:157], v[74:75], s[10:11], v[146:147] op_sel_hi:[1,0,0]
	v_pk_fma_f32 v[152:153], v[76:77], s[10:11], v[146:147] op_sel_hi:[1,0,0]
	v_pk_fma_f32 v[146:147], v[78:79], s[10:11], v[146:147] op_sel_hi:[1,0,0]
	v_fmac_f32_e32 v202, v64, v229
	s_add_i32 s2, s2, 2
	s_and_b64 vcc, exec, s[20:21]
	s_waitcnt lgkmcnt(0)
	s_barrier
	s_cbranch_vccnz .LBB0_437
	v_mov_b32_e32 v226, v162
	s_branch .LBB0_425
.LBB0_437:
	ds_read_b128 v[64:67], v209 offset:49152
	ds_read_b128 v[68:71], v209 offset:57344
	s_waitcnt lgkmcnt(1)
	v_mfma_f32_32x32x16_bf16 v[80:95], v[64:67], v[118:121], 0
	s_waitcnt lgkmcnt(0)
	v_mfma_f32_32x32x16_bf16 v[64:79], v[68:71], v[118:121], 0
	ds_read_b128 v[118:121], v221 offset:49152
	ds_read_b128 v[130:133], v221 offset:57344
	s_waitcnt lgkmcnt(1)
	v_mfma_f32_32x32x16_bf16 v[80:95], v[118:121], v[126:129], v[80:95]
	s_waitcnt lgkmcnt(0)
	v_mfma_f32_32x32x16_bf16 v[64:79], v[130:133], v[126:129], v[64:79]
	ds_read_b128 v[118:121], v222 offset:49152
	ds_read_b128 v[126:129], v222 offset:57344
	s_waitcnt lgkmcnt(1)
	v_mfma_f32_32x32x16_bf16 v[80:95], v[118:121], v[122:125], v[80:95]
	s_waitcnt lgkmcnt(0)
	v_mfma_f32_32x32x16_bf16 v[64:79], v[126:129], v[122:125], v[64:79]
	ds_read_b128 v[118:121], v210 offset:49152
	ds_read_b128 v[122:125], v210 offset:57344
	s_waitcnt lgkmcnt(1)
	v_mfma_f32_32x32x16_bf16 v[80:95], v[118:121], v[114:117], v[80:95]
	s_waitcnt lgkmcnt(0)
	v_mfma_f32_32x32x16_bf16 v[64:79], v[122:125], v[114:117], v[64:79]
	ds_read_b128 v[114:117], v211 offset:49152
	ds_read_b128 v[118:121], v211 offset:57344
	v_exp_f32_e32 v122, v146
	v_exp_f32_e32 v123, v147
	s_waitcnt lgkmcnt(1)
	v_mfma_f32_32x32x16_bf16 v[80:95], v[114:117], v[110:113], v[80:95]
	s_waitcnt lgkmcnt(0)
	v_mfma_f32_32x32x16_bf16 v[64:79], v[118:121], v[110:113], v[64:79]
	ds_read_b128 v[110:113], v223 offset:49152
	ds_read_b128 v[114:117], v223 offset:57344
	v_exp_f32_e32 v118, v156
	v_exp_f32_e32 v119, v157
	v_exp_f32_e32 v120, v152
	v_exp_f32_e32 v121, v153
	s_waitcnt lgkmcnt(1)
	v_mfma_f32_32x32x16_bf16 v[80:95], v[110:113], v[106:109], v[80:95]
	s_waitcnt lgkmcnt(0)
	v_mfma_f32_32x32x16_bf16 v[64:79], v[114:117], v[106:109], v[64:79]
	ds_read_b128 v[106:109], v225 offset:49152
	ds_read_b128 v[110:113], v225 offset:57344
	v_exp_f32_e32 v114, v150
	v_exp_f32_e32 v115, v151
	v_exp_f32_e32 v116, v148
	v_exp_f32_e32 v117, v149
	s_waitcnt lgkmcnt(1)
	v_mfma_f32_32x32x16_bf16 v[80:95], v[106:109], v[102:105], v[80:95]
	s_waitcnt lgkmcnt(0)
	v_mfma_f32_32x32x16_bf16 v[64:79], v[110:113], v[102:105], v[64:79]
	ds_read_b128 v[102:105], v224 offset:49152
	ds_read_b128 v[106:109], v224 offset:57344
	v_exp_f32_e32 v110, v158
	v_exp_f32_e32 v111, v159
	v_exp_f32_e32 v112, v154
	v_exp_f32_e32 v113, v155
	s_waitcnt lgkmcnt(1)
	v_mfma_f32_32x32x16_bf16 v[80:95], v[102:105], v[98:101], v[80:95]
	s_waitcnt lgkmcnt(0)
; #define SBAR() __builtin_amdgcn_sched_barrier(0)
; #define RESC(a) do { if (__any((a) < 1.f)) { if (hi == 0) al_l[r32] = (a); asm volatile("s_waitcnt lgkmcnt(0)" ::: "memory"); \
;     for (int d = 0; d < 4; ++d) for (int r = 0; r < 16; ++r) o[d][r] *= al_l[crow(r, hi)]; } } while (0)
; __device__ __forceinline__ void finishSM(f32x16& p0, f32x16& p1, float alpha, float& l_reg, bf16x8& pa0, bf16x8& pa1, bf16x8& pa2, bf16x8& pa3) {
;   for (int r = 0; r < 16; ++r) p1[r] = __builtin_amdgcn_exp2f(p1[r]);
;   float ps = 0; for (int r = 0; r < 16; ++r) ps += p0[r]; for (int r = 0; r < 16; ++r) ps += p1[r];
;   { auto rr = __builtin_amdgcn_permlane32_swap(__float_as_uint(ps), __float_as_uint(ps), false, false);
;     ps = __uint_as_float(rr[0]) + __uint_as_float(rr[1]); }
;   l_reg = l_reg * alpha + ps;
;     ...
;   PK4(p0, 0, pa0); PK4(p0, 8, pa1); PK4(p1, 0, pa2); PK4(p1, 8, pa3);
;     ...
; }
; template <bool HALF> __device__ __forceinline__ void dense_body(const bf16_t* __restrict__ Qb, const bf16_t* __restrict__ Kh, const bf16_t* __restrict__ Vh, ...
;     ...
;   finishSM(pA0, pA1, alA, l_reg, pa0, pa1, pa2, pa3); SBAR();
;   pv_d0(o, vb0, pa0, pa1, pa2, pa3); partialSM(pB0, pB1, m_reg, mnB, alB);
;   __syncthreads(); RESC(alB);
	v_mfma_f32_32x32x16_bf16 v[64:79], v[106:109], v[98:101], v[64:79]
	v_add_f32_e32 v98, 0, v163
	v_add_f32_e32 v98, v177, v98
	v_add_f32_e32 v98, v164, v98
	v_add_f32_e32 v98, v188, v98
	v_add_f32_e32 v98, v176, v98
	v_add_f32_e32 v98, v189, v98
	v_add_f32_e32 v98, v165, v98
	v_add_f32_e32 v98, v175, v98
	v_add_f32_e32 v98, v166, v98
	v_add_f32_e32 v98, v173, v98
	v_add_f32_e32 v98, v167, v98
	v_add_f32_e32 v98, v174, v98
	v_exp_f32_e32 v108, v160
	v_add_f32_e32 v98, v168, v98
	v_exp_f32_e32 v109, v161
	v_add_f32_e32 v98, v171, v98
	v_add_f32_e32 v98, v169, v98
	v_add_f32_e32 v98, v172, v98
	v_add_f32_e32 v98, v108, v98
	v_add_f32_e32 v98, v109, v98
	v_add_f32_e32 v98, v110, v98
	v_add_f32_e32 v98, v111, v98
	v_add_f32_e32 v98, v112, v98
	v_add_f32_e32 v98, v113, v98
	v_add_f32_e32 v98, v114, v98
	v_add_f32_e32 v98, v115, v98
	v_add_f32_e32 v98, v116, v98
	v_add_f32_e32 v98, v117, v98
	v_add_f32_e32 v98, v118, v98
	v_add_f32_e32 v98, v119, v98
	v_add_f32_e32 v98, v120, v98
	v_add_f32_e32 v98, v121, v98
	v_add_f32_e32 v98, v122, v98
	v_add_f32_e32 v102, v123, v98
	v_mov_b32_e32 v103, v102
	v_cvt_pk_bf16_f32 v98, v163, v177
	v_cvt_pk_bf16_f32 v99, v164, v188
	v_cvt_pk_bf16_f32 v100, v176, v189
	v_cvt_pk_bf16_f32 v101, v165, v175
	s_nop 1
	v_permlane32_swap_b32_e32 v102, v103
	v_permlane32_swap_b32_e32 v98, v100
	v_permlane32_swap_b32_e32 v99, v101
	v_cvt_pk_bf16_f32 v104, v166, v173
	v_cvt_pk_bf16_f32 v105, v167, v174
	v_cvt_pk_bf16_f32 v106, v168, v171
	v_cvt_pk_bf16_f32 v107, v169, v172
	v_cvt_pk_bf16_f32 v108, v108, v109
	v_cvt_pk_bf16_f32 v109, v110, v111
	v_cvt_pk_bf16_f32 v110, v112, v113
	v_cvt_pk_bf16_f32 v111, v114, v115
	v_cvt_pk_bf16_f32 v112, v116, v117
	v_cvt_pk_bf16_f32 v113, v118, v119
	v_cvt_pk_bf16_f32 v114, v120, v121
	v_cvt_pk_bf16_f32 v115, v122, v123
	s_nop 0
	v_permlane32_swap_b32_e32 v104, v106
	v_permlane32_swap_b32_e32 v105, v107
	v_permlane32_swap_b32_e32 v108, v110
	v_permlane32_swap_b32_e32 v109, v111
	v_permlane32_swap_b32_e32 v112, v114
	v_permlane32_swap_b32_e32 v113, v115
	ds_read_b64_tr_b16 v[116:117], v204 offset:0
	ds_read_b64_tr_b16 v[118:119], v204 offset:0x800
	ds_read_b64_tr_b16 v[120:121], v204 offset:0x1000
	ds_read_b64_tr_b16 v[122:123], v204 offset:0x1800
	ds_read_b64_tr_b16 v[124:125], v204 offset:0x2000
	ds_read_b64_tr_b16 v[126:127], v204 offset:0x2800
	ds_read_b64_tr_b16 v[128:129], v204 offset:0x3000
	ds_read_b64_tr_b16 v[130:131], v204 offset:0x3800
	s_waitcnt lgkmcnt(0)
	s_nop 0
	v_mfma_f32_32x32x16_bf16 v[0:15], v[98:101], v[116:119], v[0:15]
	ds_read_b64_tr_b16 v[116:117], v204 offset:0x200
	ds_read_b64_tr_b16 v[118:119], v204 offset:0xa00
	v_mfma_f32_32x32x16_bf16 v[0:15], v[104:107], v[120:123], v[0:15]
	ds_read_b64_tr_b16 v[120:121], v204 offset:0x1200
	ds_read_b64_tr_b16 v[122:123], v204 offset:0x1a00
	v_mfma_f32_32x32x16_bf16 v[0:15], v[108:111], v[124:127], v[0:15]
	ds_read_b64_tr_b16 v[124:125], v204 offset:0x2200
	ds_read_b64_tr_b16 v[126:127], v204 offset:0x2a00
	v_mfma_f32_32x32x16_bf16 v[0:15], v[112:115], v[128:131], v[0:15]
	ds_read_b64_tr_b16 v[128:129], v204 offset:0x3200
	ds_read_b64_tr_b16 v[130:131], v204 offset:0x3a00
	s_waitcnt lgkmcnt(0)
	v_mfma_f32_32x32x16_bf16 v[48:63], v[98:101], v[116:119], v[48:63]
	ds_read_b64_tr_b16 v[116:117], v204 offset:0x400
	ds_read_b64_tr_b16 v[118:119], v204 offset:0xc00
	v_mfma_f32_32x32x16_bf16 v[48:63], v[104:107], v[120:123], v[48:63]
	ds_read_b64_tr_b16 v[120:121], v204 offset:0x1400
	ds_read_b64_tr_b16 v[122:123], v204 offset:0x1c00
	v_mfma_f32_32x32x16_bf16 v[48:63], v[108:111], v[124:127], v[48:63]
	ds_read_b64_tr_b16 v[124:125], v204 offset:0x2400
	ds_read_b64_tr_b16 v[126:127], v204 offset:0x2c00
	v_mfma_f32_32x32x16_bf16 v[48:63], v[112:115], v[128:131], v[48:63]
	ds_read_b64_tr_b16 v[128:129], v204 offset:0x3400
	ds_read_b64_tr_b16 v[130:131], v204 offset:0x3c00
	s_waitcnt lgkmcnt(0)
	v_mfma_f32_32x32x16_bf16 v[32:47], v[98:101], v[116:119], v[32:47]
	ds_read_b64_tr_b16 v[116:117], v204 offset:0x600
	ds_read_b64_tr_b16 v[118:119], v204 offset:0xe00
	v_mfma_f32_32x32x16_bf16 v[32:47], v[104:107], v[120:123], v[32:47]
	ds_read_b64_tr_b16 v[120:121], v204 offset:0x1600
	ds_read_b64_tr_b16 v[122:123], v204 offset:0x1e00
	v_mfma_f32_32x32x16_bf16 v[32:47], v[108:111], v[124:127], v[32:47]
	ds_read_b64_tr_b16 v[124:125], v204 offset:0x2600
	ds_read_b64_tr_b16 v[126:127], v204 offset:0x2e00
	v_mfma_f32_32x32x16_bf16 v[32:47], v[112:115], v[128:131], v[32:47]
	ds_read_b64_tr_b16 v[128:129], v204 offset:0x3600
	ds_read_b64_tr_b16 v[130:131], v204 offset:0x3e00
	s_waitcnt lgkmcnt(0)
	v_mfma_f32_32x32x16_bf16 v[16:31], v[98:101], v[116:119], v[16:31]
	v_max_f32_e32 v98, v81, v81
	v_max_f32_e32 v99, v80, v80
	v_max_f32_e32 v98, v99, v98
	v_max3_f32 v98, v98, v82, v83
	v_max3_f32 v98, v98, v84, v85
	v_max3_f32 v98, v98, v86, v87
	v_max3_f32 v98, v98, v88, v89
	v_max3_f32 v98, v98, v90, v91
	v_max3_f32 v98, v98, v92, v93
	v_mfma_f32_32x32x16_bf16 v[16:31], v[104:107], v[120:123], v[16:31]
	v_max3_f32 v98, v98, v94, v95
	v_max3_f32 v98, v98, v64, v65
	v_max3_f32 v98, v98, v66, v67
	v_max3_f32 v98, v98, v68, v69
	v_max3_f32 v98, v98, v70, v71
	v_max3_f32 v98, v98, v72, v73
	v_max3_f32 v98, v98, v74, v75
	v_max3_f32 v98, v98, v76, v77
	v_mfma_f32_32x32x16_bf16 v[16:31], v[108:111], v[124:127], v[16:31]
	v_max3_f32 v98, v98, v78, v79
	v_mov_b32_e32 v99, v98
	s_nop 1
	v_permlane32_swap_b32_e32 v98, v99
	v_max_f32_e32 v99, v99, v99
	v_max_f32_e32 v98, v98, v98
	v_max_f32_e32 v98, v98, v99
	v_sub_f32_e32 v99, v98, v170
	v_cmp_ge_f32_e32 vcc, s87, v99
	v_max_f32_e32 v99, v170, v170
	v_max_f32_e32 v99, v99, v98
	v_mfma_f32_32x32x16_bf16 v[16:31], v[112:115], v[128:131], v[16:31]
	v_sub_f32_e32 v98, v170, v99
	v_mul_f32_e32 v98, 0x3e0293ee, v98
	v_exp_f32_e32 v98, v98
	s_cmp_eq_u64 vcc, exec
	s_cselect_b64 s[42:43], -1, 0
	v_cndmask_b32_e64 v98, v98, 1.0, s[42:43]
	v_cmp_gt_f32_e32 vcc, 1.0, v98
	s_waitcnt vmcnt(0)
	s_barrier
; #define RESC(a) do { if (__any((a) < 1.f)) { if (hi == 0) al_l[r32] = (a); asm volatile("s_waitcnt lgkmcnt(0)" ::: "memory"); \
;     for (int d = 0; d < 4; ++d) for (int r = 0; r < 16; ++r) o[d][r] *= al_l[crow(r, hi)]; } } while (0)
; template <bool HALF> __device__ __forceinline__ void dense_body(const bf16_t* __restrict__ Qb, const bf16_t* __restrict__ Kh, const bf16_t* __restrict__ Vh, ...
;     ...
;   __syncthreads(); RESC(alB);
	s_cbranch_vccz .LBB0_441
	s_and_saveexec_b64 s[6:7], s[40:41]
	ds_write_b32 v201, v98 offset:128
	s_or_b64 exec, exec, s[6:7]
	s_waitcnt lgkmcnt(0)
	v_add_u32_e32 v100, v200, v96
	ds_read_b128 v[104:107], v100 offset:224
	ds_read_b128 v[108:111], v100 offset:192
	ds_read_b128 v[112:115], v100 offset:160
	ds_read_b128 v[116:119], v100 offset:128
	s_waitcnt lgkmcnt(3)
	v_pk_mul_f32 v[12:13], v[12:13], v[104:105]
	s_waitcnt lgkmcnt(2)
	v_pk_mul_f32 v[8:9], v[8:9], v[108:109]
	s_waitcnt lgkmcnt(1)
	v_pk_mul_f32 v[4:5], v[4:5], v[112:113]
	v_pk_mul_f32 v[14:15], v[14:15], v[106:107]
	v_pk_mul_f32 v[10:11], v[10:11], v[110:111]
	v_pk_mul_f32 v[6:7], v[6:7], v[114:115]
	s_waitcnt lgkmcnt(0)
	v_pk_mul_f32 v[2:3], v[2:3], v[118:119]
	v_pk_mul_f32 v[0:1], v[0:1], v[116:117]
	v_pk_mul_f32 v[60:61], v[60:61], v[104:105]
	v_pk_mul_f32 v[56:57], v[56:57], v[108:109]
	v_pk_mul_f32 v[52:53], v[52:53], v[112:113]
	v_pk_mul_f32 v[62:63], v[62:63], v[106:107]
	v_pk_mul_f32 v[58:59], v[58:59], v[110:111]
	v_pk_mul_f32 v[54:55], v[54:55], v[114:115]
	v_pk_mul_f32 v[50:51], v[50:51], v[118:119]
	v_pk_mul_f32 v[48:49], v[48:49], v[116:117]
	v_pk_mul_f32 v[44:45], v[44:45], v[104:105]
	v_pk_mul_f32 v[40:41], v[40:41], v[108:109]
	v_pk_mul_f32 v[36:37], v[36:37], v[112:113]
	v_pk_mul_f32 v[46:47], v[46:47], v[106:107]
	v_pk_mul_f32 v[42:43], v[42:43], v[110:111]
	v_pk_mul_f32 v[38:39], v[38:39], v[114:115]
	v_pk_mul_f32 v[34:35], v[34:35], v[118:119]
	v_pk_mul_f32 v[32:33], v[32:33], v[116:117]
	v_pk_mul_f32 v[28:29], v[28:29], v[104:105]
	v_pk_mul_f32 v[24:25], v[24:25], v[108:109]
	v_pk_mul_f32 v[20:21], v[20:21], v[112:113]
	v_pk_mul_f32 v[30:31], v[30:31], v[106:107]
	v_pk_mul_f32 v[26:27], v[26:27], v[110:111]
	v_pk_mul_f32 v[22:23], v[22:23], v[114:115]
	v_pk_mul_f32 v[18:19], v[18:19], v[118:119]
	v_pk_mul_f32 v[16:17], v[16:17], v[116:117]
